# PEER V pass: the token's four sum-of-squares slots written by lanes 0-3 with one store instead of four single-lane stores
# baseline (speedup 1.0000x reference)
; __device__ __forceinline__ void phase_peer_v(Frame& F, bf16_t* XB, const unsigned short* EID, const unsigned char* ACO8, const float* ASC, const unsigned char* V4S, float* SSQP) {
;     ...
;     for (; t < TOK; t += step) {
;         const int tn = (t + step < TOK) ? t + step : t, tnn = (t + 2 * step < TOK) ? t + 2 * step : t;
;         u32x4 aB; unsigned evC; u32x2 xfB, scB;
;         { const unsigned short* ep = EID + (size_t)tnn * 128 + i16 + 2 * c; const unsigned char* ap = ACO8 + (size_t)tn * 128 + i16; const bf16_t* xp = XB + (size_t)tn * DM + col; const float* sp = ASC + 2 * (size_t)tn;
;           GLD4(evC, ep); GLD16(aB, ap); GLD8(xfB, xp); GLD8(scB, sp); }
;         int oL[16], oP[16];
; #pragma unroll
;         for (int w = 0; w < 16; w += 4) {
;             asm volatile("s_waitcnt vmcnt(16)" : "+v"(vw[w]), "+v"(vw[w + 1]), "+v"(vw[w + 2]), "+v"(vw[w + 3]) :: "memory");
;             const int a4 = (int)aA[w >> 2];
; #pragma unroll
;             for (int k = 0; k < 4; ++k) { const unsigned d0 = vw[w][k], d1 = vw[w + 1][k], d2 = vw[w + 2][k], d3 = vw[w + 3][k];
;                 const unsigned q01l = __builtin_amdgcn_perm(d1, d0, 0x05010400u), q01h = __builtin_amdgcn_perm(d1, d0, 0x07030602u), q23l = __builtin_amdgcn_perm(d3, d2, 0x05010400u), q23h = __builtin_amdgcn_perm(d3, d2, 0x07030602u);
;                 const int t0 = (int)__builtin_amdgcn_perm(q23l, q01l, 0x05040100u), t1 = (int)__builtin_amdgcn_perm(q23l, q01l, 0x07060302u), t2 = (int)__builtin_amdgcn_perm(q23h, q01h, 0x05040100u), t3 = (int)__builtin_amdgcn_perm(q23h, q01h, 0x07060302u);
;                 const int l0 = t0 & 0x0f0f0f0f, l1 = t1 & 0x0f0f0f0f, l2 = t2 & 0x0f0f0f0f, l3 = t3 & 0x0f0f0f0f;
;                 if (w == 0) { oL[4 * k] = sdot4_z(l0, a4); oL[4 * k + 1] = sdot4_z(l1, a4); oL[4 * k + 2] = sdot4_z(l2, a4); oL[4 * k + 3] = sdot4_z(l3, a4);
;                               oP[4 * k] = sdot4_z(t0, a4); oP[4 * k + 1] = sdot4_z(t1, a4); oP[4 * k + 2] = sdot4_z(t2, a4); oP[4 * k + 3] = sdot4_z(t3, a4); }
;                 else { oL[4 * k]     = __builtin_amdgcn_sdot4(l0, a4, oL[4 * k], false);     oL[4 * k + 1] = __builtin_amdgcn_sdot4(l1, a4, oL[4 * k + 1], false);
;                        oL[4 * k + 2] = __builtin_amdgcn_sdot4(l2, a4, oL[4 * k + 2], false); oL[4 * k + 3] = __builtin_amdgcn_sdot4(l3, a4, oL[4 * k + 3], false);
.LBB0_1008:
	s_mov_b32 s21, s10
	s_add_i32 s10, s10, s6
	s_cmpk_gt_i32 s10, 0x7fff
	s_cselect_b64 s[18:19], -1, 0
	s_cmp_lt_i32 s10, 0x8000
	s_cselect_b32 s20, s10, s21
	s_add_i32 s26, s7, s21
	s_cmp_lt_i32 s26, 0x8000
	s_cselect_b32 s26, s26, s21
	s_ashr_i32 s27, s26, 31
	s_lshl_b64 s[26:27], s[26:27], 8
	s_ashr_i32 s21, s20, 31
	v_lshl_add_u64 v[68:69], v[78:79], 0, s[26:27]
	s_lshl_b64 s[26:27], s[20:21], 7
	v_lshl_add_u64 v[70:71], v[80:81], 0, s[26:27]
	s_lshl_b64 s[26:27], s[20:21], 11
	s_lshl_b64 s[20:21], s[20:21], 3
	s_add_u32 s20, s66, s20
	global_load_dword v92, v[68:69], off
	v_lshl_add_u64 v[86:87], v[82:83], 0, s[26:27]
	s_addc_u32 s21, s67, s21
	global_load_dwordx4 v[68:71], v[70:71], off
	global_load_dwordx2 v[86:87], v[86:87], off
	v_mov_b64_e32 v[88:89], s[20:21]
	global_load_dwordx2 v[88:89], v[88:89], off
	s_waitcnt vmcnt(16)
	s_nop 0
	v_perm_b32 v93, v16, v8, s11
	v_perm_b32 v94, v4, v0, s11
	v_perm_b32 v97, v93, v94, s23
	v_perm_b32 v8, v16, v8, s25
	v_perm_b32 v0, v4, v0, s25
	v_and_b32_e32 v95, 0xf0f0f0f, v97
	v_perm_b32 v4, v8, v0, s23
	v_perm_b32 v0, v8, v0, s24
	v_and_b32_e32 v16, 0xf0f0f0f, v4
	v_and_b32_e32 v8, 0xf0f0f0f, v0
	v_dot4_i32_i8 v101, v95, v64, 0
	v_dot4_i32_i8 v96, v0, v64, 0
	v_dot4_i32_i8 v95, v4, v64, 0
	v_perm_b32 v0, v17, v9, s11
	v_perm_b32 v4, v5, v1, s11
	v_perm_b32 v9, v17, v9, s25
	v_perm_b32 v1, v5, v1, s25
	v_dot4_i32_i8 v104, v8, v64, 0
	v_perm_b32 v8, v0, v4, s23
	v_perm_b32 v0, v0, v4, s24
	v_perm_b32 v5, v9, v1, s23
	v_perm_b32 v1, v9, v1, s24
	v_perm_b32 v93, v93, v94, s24
	v_and_b32_e32 v4, 0xf0f0f0f, v0
	v_and_b32_e32 v9, 0xf0f0f0f, v1
	v_dot4_i32_i8 v100, v1, v64, 0
	v_dot4_i32_i8 v98, v0, v64, 0
	v_perm_b32 v0, v18, v10, s11
	v_perm_b32 v1, v6, v2, s11
	v_and_b32_e32 v94, 0xf0f0f0f, v93
	v_dot4_i32_i8 v108, v4, v64, 0
	v_perm_b32 v4, v0, v1, s23
	v_perm_b32 v0, v0, v1, s24
	v_dot4_i32_i8 v103, v16, v64, 0
	v_dot4_i32_i8 v102, v94, v64, 0
	v_dot4_i32_i8 v94, v93, v64, 0
	v_dot4_i32_i8 v93, v97, v64, 0
	v_and_b32_e32 v16, 0xf0f0f0f, v8
	v_dot4_i32_i8 v97, v8, v64, 0
	v_and_b32_e32 v1, 0xf0f0f0f, v0
	v_perm_b32 v8, v18, v10, s25
	v_perm_b32 v2, v6, v2, s25
	v_perm_b32 v6, v8, v2, s23
	v_perm_b32 v2, v8, v2, s24
	v_dot4_i32_i8 v117, v1, v64, 0
	v_dot4_i32_i8 v107, v0, v64, 0
	v_perm_b32 v0, v19, v11, s11
	v_perm_b32 v1, v7, v3, s11
	v_and_b32_e32 v8, 0xf0f0f0f, v2
	v_dot4_i32_i8 v111, v2, v64, 0
	v_perm_b32 v2, v0, v1, s23
	v_perm_b32 v0, v0, v1, s24
	v_and_b32_e32 v17, 0xf0f0f0f, v5
	v_dot4_i32_i8 v99, v5, v64, 0
	v_and_b32_e32 v5, 0xf0f0f0f, v4
	v_and_b32_e32 v1, 0xf0f0f0f, v0
	v_dot4_i32_i8 v113, v0, v64, 0
	v_mov_b32_e32 v0, 0
	v_dot4_i32_i8 v116, v5, v64, 0
	v_perm_b32 v5, v19, v11, s25
	v_perm_b32 v3, v7, v3, s25
	v_dot4_i32_i8 v121, v1, v64, 0
	v_mov_b32_dpp v0, v91 row_newbcast:0 row_mask:0xf bank_mask:0x3
	v_mov_b32_e32 v1, 0
	v_dot4_i32_i8 v112, v9, v64, 0
	v_and_b32_e32 v9, 0xf0f0f0f, v6
	v_dot4_i32_i8 v109, v6, v64, 0
	v_perm_b32 v6, v5, v3, s23
	v_perm_b32 v3, v5, v3, s24
	v_mov_b32_dpp v0, v91 row_newbcast:8 row_mask:0xf bank_mask:0xc
	v_mov_b32_dpp v1, v91 row_newbcast:1 row_mask:0xf bank_mask:0x3
	v_dot4_i32_i8 v110, v17, v64, 0
	v_dot4_i32_i8 v106, v16, v64, 0
	v_dot4_i32_i8 v119, v8, v64, 0
	v_dot4_i32_i8 v118, v9, v64, 0
	v_dot4_i32_i8 v105, v4, v64, 0
	v_and_b32_e32 v4, 0xf0f0f0f, v2
	v_and_b32_e32 v7, 0xf0f0f0f, v6
	v_and_b32_e32 v5, 0xf0f0f0f, v3
	v_dot4_i32_i8 v123, v5, v64, 0
	v_dot4_i32_i8 v122, v7, v64, 0
	v_dot4_i32_i8 v120, v4, v64, 0
	v_dot4_i32_i8 v115, v3, v64, 0
	v_dot4_i32_i8 v114, v6, v64, 0
	v_dot4_i32_i8 v64, v2, v64, 0
	v_mov_b32_dpp v1, v91 row_newbcast:9 row_mask:0xf bank_mask:0xc
	v_lshlrev_b32_e32 v2, 7, v0
	v_bfe_u32 v0, v0, 16, 16
	v_lshl_or_b32 v4, v0, 7, v90
	v_lshlrev_b32_e32 v0, 7, v1
	v_and_or_b32 v2, v2, s22, v90
	v_and_or_b32 v8, v0, s22, v90
	v_bfe_u32 v0, v1, 16, 16
	v_lshl_or_b32 v16, v0, 7, v90
	global_load_dwordx4 v[0:3], v2, s[8:9]
	global_load_dwordx4 v[4:7], v4, s[8:9]
	global_load_dwordx4 v[8:11], v8, s[8:9]
	global_load_dwordx4 v[16:19], v16, s[8:9]
	s_waitcnt vmcnt(16)
	s_nop 0
	v_perm_b32 v124, v36, v28, s11
	v_perm_b32 v125, v20, v12, s11
	v_perm_b32 v28, v36, v28, s25
	v_perm_b32 v12, v20, v12, s25
	v_perm_b32 v20, v28, v12, s23
	v_perm_b32 v12, v28, v12, s24
	v_and_b32_e32 v36, 0xf0f0f0f, v20
	v_and_b32_e32 v28, 0xf0f0f0f, v12
	v_dot4c_i32_i8_e32 v96, v12, v65
	v_dot4c_i32_i8_e32 v95, v20, v65
	v_perm_b32 v12, v37, v29, s11
	v_perm_b32 v20, v21, v13, s11
	v_perm_b32 v29, v37, v29, s25
	v_perm_b32 v13, v21, v13, s25
	v_dot4c_i32_i8_e32 v104, v28, v65
	v_perm_b32 v28, v12, v20, s23
	v_perm_b32 v12, v12, v20, s24
	v_perm_b32 v21, v29, v13, s23
	v_perm_b32 v13, v29, v13, s24
	v_and_b32_e32 v20, 0xf0f0f0f, v12
	v_and_b32_e32 v29, 0xf0f0f0f, v13
	v_dot4c_i32_i8_e32 v100, v13, v65
	v_dot4c_i32_i8_e32 v98, v12, v65
	v_perm_b32 v12, v38, v30, s11
	v_perm_b32 v13, v22, v14, s11
	v_dot4c_i32_i8_e32 v108, v20, v65
	v_perm_b32 v20, v12, v13, s23
	v_perm_b32 v12, v12, v13, s24
	v_dot4c_i32_i8_e32 v103, v36, v65
	v_and_b32_e32 v36, 0xf0f0f0f, v28
	v_dot4c_i32_i8_e32 v97, v28, v65
	v_and_b32_e32 v13, 0xf0f0f0f, v12
	v_perm_b32 v28, v38, v30, s25
	v_perm_b32 v14, v22, v14, s25
	v_perm_b32 v22, v28, v14, s23
	v_perm_b32 v14, v28, v14, s24
	v_dot4c_i32_i8_e32 v117, v13, v65
	v_dot4c_i32_i8_e32 v107, v12, v65
	v_perm_b32 v12, v39, v31, s11
	v_perm_b32 v13, v23, v15, s11
	v_and_b32_e32 v37, 0xf0f0f0f, v21
	v_dot4c_i32_i8_e32 v99, v21, v65
	v_and_b32_e32 v21, 0xf0f0f0f, v20
	v_and_b32_e32 v28, 0xf0f0f0f, v14
	v_dot4c_i32_i8_e32 v111, v14, v65
	v_dot4c_i32_i8_e32 v105, v20, v65
	v_perm_b32 v14, v12, v13, s23
	v_perm_b32 v20, v39, v31, s25
; #define PEER_BC(ev_, cp_) peer_bc((ev_), (cp_))
; __device__ __forceinline__ void phase_peer_v(Frame& F, bf16_t* XB, const unsigned short* EID, const unsigned char* ACO8, const float* ASC, const unsigned char* V4S, float* SSQP) {
;     ...
;         for (int w = 0; w < 16; w += 4) {
;             asm volatile("s_waitcnt vmcnt(16)" : "+v"(vw[w]), "+v"(vw[w + 1]), "+v"(vw[w + 2]), "+v"(vw[w + 3]) :: "memory");
;             const int a4 = (int)aA[w >> 2];
; #pragma unroll
;             for (int k = 0; k < 4; ++k) { const unsigned d0 = vw[w][k], d1 = vw[w + 1][k], d2 = vw[w + 2][k], d3 = vw[w + 3][k];
;                 const unsigned q01l = __builtin_amdgcn_perm(d1, d0, 0x05010400u), q01h = __builtin_amdgcn_perm(d1, d0, 0x07030602u), q23l = __builtin_amdgcn_perm(d3, d2, 0x05010400u), q23h = __builtin_amdgcn_perm(d3, d2, 0x07030602u);
;                 const int t0 = (int)__builtin_amdgcn_perm(q23l, q01l, 0x05040100u), t1 = (int)__builtin_amdgcn_perm(q23l, q01l, 0x07060302u), t2 = (int)__builtin_amdgcn_perm(q23h, q01h, 0x05040100u), t3 = (int)__builtin_amdgcn_perm(q23h, q01h, 0x07060302u);
;                 const int l0 = t0 & 0x0f0f0f0f, l1 = t1 & 0x0f0f0f0f, l2 = t2 & 0x0f0f0f0f, l3 = t3 & 0x0f0f0f0f;
;                 if (w == 0) { oL[4 * k] = sdot4_z(l0, a4); oL[4 * k + 1] = sdot4_z(l1, a4); oL[4 * k + 2] = sdot4_z(l2, a4); oL[4 * k + 3] = sdot4_z(l3, a4);
;                               oP[4 * k] = sdot4_z(t0, a4); oP[4 * k + 1] = sdot4_z(t1, a4); oP[4 * k + 2] = sdot4_z(t2, a4); oP[4 * k + 3] = sdot4_z(t3, a4); }
;                 else { oL[4 * k]     = __builtin_amdgcn_sdot4(l0, a4, oL[4 * k], false);     oL[4 * k + 1] = __builtin_amdgcn_sdot4(l1, a4, oL[4 * k + 1], false);
;                        oL[4 * k + 2] = __builtin_amdgcn_sdot4(l2, a4, oL[4 * k + 2], false); oL[4 * k + 3] = __builtin_amdgcn_sdot4(l3, a4, oL[4 * k + 3], false);
;                        oP[4 * k]     = __builtin_amdgcn_sdot4(t0, a4, oP[4 * k], false);     oP[4 * k + 1] = __builtin_amdgcn_sdot4(t1, a4, oP[4 * k + 1], false);
;                        oP[4 * k + 2] = __builtin_amdgcn_sdot4(t2, a4, oP[4 * k + 2], false); oP[4 * k + 3] = __builtin_amdgcn_sdot4(t3, a4, oP[4 * k + 3], false); } }
;             PIN16(oL); PIN16(oP);
;             { const unsigned bc0 = PEER_BC(evB, w >> 1), bc1 = PEER_BC(evB, (w >> 1) + 1);
	v_perm_b32 v15, v23, v15, s25
	v_dot4c_i32_i8_e32 v116, v21, v65
	v_perm_b32 v21, v20, v15, s24
	v_perm_b32 v12, v12, v13, s24
	v_and_b32_e32 v13, 0xf0f0f0f, v14
	v_perm_b32 v15, v20, v15, s23
	v_dot4c_i32_i8_e32 v113, v12, v65
	v_dot4c_i32_i8_e32 v120, v13, v65
	v_and_b32_e32 v13, 0xf0f0f0f, v21
	v_and_b32_e32 v12, 0xf0f0f0f, v12
	v_dot4c_i32_i8_e32 v123, v13, v65
	v_and_b32_e32 v13, 0xf0f0f0f, v15
	v_dot4c_i32_i8_e32 v121, v12, v65
	v_mov_b32_e32 v12, 0
	v_dot4c_i32_i8_e32 v122, v13, v65
	v_mov_b32_e32 v13, 0
	v_mov_b32_dpp v12, v91 row_newbcast:2 row_mask:0xf bank_mask:0x3
	v_perm_b32 v126, v124, v125, s23
	v_mov_b32_dpp v13, v91 row_newbcast:3 row_mask:0xf bank_mask:0x3
	v_mov_b32_dpp v12, v91 row_newbcast:10 row_mask:0xf bank_mask:0xc
	v_perm_b32 v124, v124, v125, s24
	v_dot4c_i32_i8_e32 v64, v14, v65
	v_mov_b32_dpp v13, v91 row_newbcast:11 row_mask:0xf bank_mask:0xc
	v_lshlrev_b32_e32 v14, 7, v12
	v_bfe_u32 v12, v12, 16, 16
	v_and_b32_e32 v127, 0xf0f0f0f, v126
	v_and_b32_e32 v125, 0xf0f0f0f, v124
	v_dot4c_i32_i8_e32 v112, v29, v65
	v_and_b32_e32 v29, 0xf0f0f0f, v22
	v_lshl_or_b32 v20, v12, 7, v90
	v_lshlrev_b32_e32 v12, 7, v13
	v_dot4c_i32_i8_e32 v102, v125, v65
	v_dot4c_i32_i8_e32 v101, v127, v65
	v_dot4c_i32_i8_e32 v94, v124, v65
	v_dot4c_i32_i8_e32 v93, v126, v65
	v_dot4c_i32_i8_e32 v110, v37, v65
	v_dot4c_i32_i8_e32 v106, v36, v65
	v_dot4c_i32_i8_e32 v119, v28, v65
	v_dot4c_i32_i8_e32 v118, v29, v65
	v_dot4c_i32_i8_e32 v109, v22, v65
	v_dot4c_i32_i8_e32 v115, v21, v65
	v_dot4c_i32_i8_e32 v114, v15, v65
	v_and_or_b32 v14, v14, s22, v90
	v_and_or_b32 v28, v12, s22, v90
	v_bfe_u32 v12, v13, 16, 16
	v_lshl_or_b32 v36, v12, 7, v90
	global_load_dwordx4 v[12:15], v14, s[8:9]
	global_load_dwordx4 v[20:23], v20, s[8:9]
	global_load_dwordx4 v[28:31], v28, s[8:9]
	global_load_dwordx4 v[36:39], v36, s[8:9]
	s_waitcnt vmcnt(16)
	s_nop 0
	v_perm_b32 v65, v52, v44, s11
	v_perm_b32 v124, v32, v24, s11
	v_perm_b32 v44, v52, v44, s25
	v_perm_b32 v24, v32, v24, s25
	v_perm_b32 v32, v44, v24, s23
	v_perm_b32 v24, v44, v24, s24
	v_and_b32_e32 v52, 0xf0f0f0f, v32
	v_and_b32_e32 v44, 0xf0f0f0f, v24
	v_dot4c_i32_i8_e32 v96, v24, v66
	v_dot4c_i32_i8_e32 v95, v32, v66
	v_perm_b32 v24, v53, v45, s11
	v_perm_b32 v32, v33, v25, s11
	v_perm_b32 v45, v53, v45, s25
	v_perm_b32 v25, v33, v25, s25
	v_dot4c_i32_i8_e32 v104, v44, v66
	v_perm_b32 v44, v24, v32, s23
	v_perm_b32 v24, v24, v32, s24
	v_perm_b32 v33, v45, v25, s23
	v_perm_b32 v25, v45, v25, s24
	v_and_b32_e32 v32, 0xf0f0f0f, v24
	v_and_b32_e32 v45, 0xf0f0f0f, v25
	v_dot4c_i32_i8_e32 v100, v25, v66
	v_dot4c_i32_i8_e32 v98, v24, v66
	v_perm_b32 v24, v54, v46, s11
	v_perm_b32 v25, v34, v26, s11
	v_dot4c_i32_i8_e32 v108, v32, v66
	v_perm_b32 v32, v24, v25, s23
	v_perm_b32 v24, v24, v25, s24
	v_dot4c_i32_i8_e32 v103, v52, v66
	v_and_b32_e32 v52, 0xf0f0f0f, v44
	v_dot4c_i32_i8_e32 v97, v44, v66
	v_and_b32_e32 v25, 0xf0f0f0f, v24
	v_perm_b32 v44, v54, v46, s25
	v_perm_b32 v26, v34, v26, s25
	v_perm_b32 v34, v44, v26, s23
	v_perm_b32 v26, v44, v26, s24
	v_dot4c_i32_i8_e32 v117, v25, v66
	v_dot4c_i32_i8_e32 v107, v24, v66
	v_perm_b32 v24, v55, v47, s11
	v_perm_b32 v25, v35, v27, s11
	v_and_b32_e32 v53, 0xf0f0f0f, v33
	v_dot4c_i32_i8_e32 v99, v33, v66
	v_and_b32_e32 v33, 0xf0f0f0f, v32
	v_and_b32_e32 v44, 0xf0f0f0f, v26
	v_dot4c_i32_i8_e32 v111, v26, v66
	v_dot4c_i32_i8_e32 v105, v32, v66
	v_perm_b32 v26, v24, v25, s23
	v_perm_b32 v32, v55, v47, s25
	v_perm_b32 v27, v35, v27, s25
	v_dot4c_i32_i8_e32 v116, v33, v66
	v_perm_b32 v33, v32, v27, s24
	v_perm_b32 v24, v24, v25, s24
	v_and_b32_e32 v25, 0xf0f0f0f, v26
	v_perm_b32 v27, v32, v27, s23
	v_dot4c_i32_i8_e32 v113, v24, v66
	v_dot4c_i32_i8_e32 v120, v25, v66
	v_and_b32_e32 v25, 0xf0f0f0f, v33
	v_and_b32_e32 v24, 0xf0f0f0f, v24
	v_dot4c_i32_i8_e32 v123, v25, v66
	v_and_b32_e32 v25, 0xf0f0f0f, v27
	v_dot4c_i32_i8_e32 v121, v24, v66
	v_mov_b32_e32 v24, 0
	v_dot4c_i32_i8_e32 v122, v25, v66
	v_mov_b32_e32 v25, 0
	v_mov_b32_dpp v24, v91 row_newbcast:4 row_mask:0xf bank_mask:0x3
	v_perm_b32 v125, v65, v124, s23
	v_mov_b32_dpp v25, v91 row_newbcast:5 row_mask:0xf bank_mask:0x3
	v_mov_b32_dpp v24, v91 row_newbcast:12 row_mask:0xf bank_mask:0xc
	v_perm_b32 v65, v65, v124, s24
	v_dot4c_i32_i8_e32 v64, v26, v66
	v_mov_b32_dpp v25, v91 row_newbcast:13 row_mask:0xf bank_mask:0xc
	v_lshlrev_b32_e32 v26, 7, v24
	v_bfe_u32 v24, v24, 16, 16
	v_and_b32_e32 v126, 0xf0f0f0f, v125
	v_and_b32_e32 v124, 0xf0f0f0f, v65
	v_dot4c_i32_i8_e32 v112, v45, v66
	v_and_b32_e32 v45, 0xf0f0f0f, v34
	v_lshl_or_b32 v32, v24, 7, v90
	v_lshlrev_b32_e32 v24, 7, v25
	v_dot4c_i32_i8_e32 v102, v124, v66
	v_dot4c_i32_i8_e32 v101, v126, v66
	v_dot4c_i32_i8_e32 v94, v65, v66
	v_dot4c_i32_i8_e32 v93, v125, v66
	v_dot4c_i32_i8_e32 v110, v53, v66
	v_dot4c_i32_i8_e32 v106, v52, v66
	v_dot4c_i32_i8_e32 v119, v44, v66
	v_dot4c_i32_i8_e32 v118, v45, v66
	v_dot4c_i32_i8_e32 v109, v34, v66
	v_dot4c_i32_i8_e32 v115, v33, v66
	v_dot4c_i32_i8_e32 v114, v27, v66
	v_and_or_b32 v26, v26, s22, v90
	v_and_or_b32 v44, v24, s22, v90
	v_bfe_u32 v24, v25, 16, 16
	v_lshl_or_b32 v52, v24, 7, v90
	global_load_dwordx4 v[24:27], v26, s[8:9]
	global_load_dwordx4 v[32:35], v32, s[8:9]
	global_load_dwordx4 v[44:47], v44, s[8:9]
	global_load_dwordx4 v[52:55], v52, s[8:9]
	s_waitcnt vmcnt(16)
; #define PEER_BC(ev_, cp_) peer_bc((ev_), (cp_))
; __device__ __forceinline__ void phase_peer_v(Frame& F, bf16_t* XB, const unsigned short* EID, const unsigned char* ACO8, const float* ASC, const unsigned char* V4S, float* SSQP) {
;     ...
;         for (int w = 0; w < 16; w += 4) {
;             asm volatile("s_waitcnt vmcnt(16)" : "+v"(vw[w]), "+v"(vw[w + 1]), "+v"(vw[w + 2]), "+v"(vw[w + 3]) :: "memory");
;             const int a4 = (int)aA[w >> 2];
; #pragma unroll
;             for (int k = 0; k < 4; ++k) { const unsigned d0 = vw[w][k], d1 = vw[w + 1][k], d2 = vw[w + 2][k], d3 = vw[w + 3][k];
;                 const unsigned q01l = __builtin_amdgcn_perm(d1, d0, 0x05010400u), q01h = __builtin_amdgcn_perm(d1, d0, 0x07030602u), q23l = __builtin_amdgcn_perm(d3, d2, 0x05010400u), q23h = __builtin_amdgcn_perm(d3, d2, 0x07030602u);
;                 const int t0 = (int)__builtin_amdgcn_perm(q23l, q01l, 0x05040100u), t1 = (int)__builtin_amdgcn_perm(q23l, q01l, 0x07060302u), t2 = (int)__builtin_amdgcn_perm(q23h, q01h, 0x05040100u), t3 = (int)__builtin_amdgcn_perm(q23h, q01h, 0x07060302u);
;                 const int l0 = t0 & 0x0f0f0f0f, l1 = t1 & 0x0f0f0f0f, l2 = t2 & 0x0f0f0f0f, l3 = t3 & 0x0f0f0f0f;
;                 if (w == 0) { oL[4 * k] = sdot4_z(l0, a4); oL[4 * k + 1] = sdot4_z(l1, a4); oL[4 * k + 2] = sdot4_z(l2, a4); oL[4 * k + 3] = sdot4_z(l3, a4);
;                               oP[4 * k] = sdot4_z(t0, a4); oP[4 * k + 1] = sdot4_z(t1, a4); oP[4 * k + 2] = sdot4_z(t2, a4); oP[4 * k + 3] = sdot4_z(t3, a4); }
;                 else { oL[4 * k]     = __builtin_amdgcn_sdot4(l0, a4, oL[4 * k], false);     oL[4 * k + 1] = __builtin_amdgcn_sdot4(l1, a4, oL[4 * k + 1], false);
;                        oL[4 * k + 2] = __builtin_amdgcn_sdot4(l2, a4, oL[4 * k + 2], false); oL[4 * k + 3] = __builtin_amdgcn_sdot4(l3, a4, oL[4 * k + 3], false);
;                        oP[4 * k]     = __builtin_amdgcn_sdot4(t0, a4, oP[4 * k], false);     oP[4 * k + 1] = __builtin_amdgcn_sdot4(t1, a4, oP[4 * k + 1], false);
;                        oP[4 * k + 2] = __builtin_amdgcn_sdot4(t2, a4, oP[4 * k + 2], false); oP[4 * k + 3] = __builtin_amdgcn_sdot4(t3, a4, oP[4 * k + 3], false); } }
;             PIN16(oL); PIN16(oP);
;             { const unsigned bc0 = PEER_BC(evB, w >> 1), bc1 = PEER_BC(evB, (w >> 1) + 1);
	s_nop 0
	v_perm_b32 v65, v60, v56, s11
	v_perm_b32 v66, v48, v40, s11
	v_perm_b32 v56, v60, v56, s25
	v_perm_b32 v40, v48, v40, s25
	v_perm_b32 v48, v56, v40, s23
	v_perm_b32 v40, v56, v40, s24
	v_and_b32_e32 v60, 0xf0f0f0f, v48
	v_and_b32_e32 v56, 0xf0f0f0f, v40
	v_dot4c_i32_i8_e32 v96, v40, v67
	v_dot4c_i32_i8_e32 v95, v48, v67
	v_perm_b32 v40, v61, v57, s11
	v_perm_b32 v48, v49, v41, s11
	v_perm_b32 v57, v61, v57, s25
	v_perm_b32 v41, v49, v41, s25
	v_dot4c_i32_i8_e32 v104, v56, v67
	v_perm_b32 v56, v40, v48, s23
	v_perm_b32 v40, v40, v48, s24
	v_perm_b32 v49, v57, v41, s23
	v_perm_b32 v41, v57, v41, s24
	v_and_b32_e32 v48, 0xf0f0f0f, v40
	v_and_b32_e32 v57, 0xf0f0f0f, v41
	v_dot4c_i32_i8_e32 v100, v41, v67
	v_dot4c_i32_i8_e32 v98, v40, v67
	v_perm_b32 v40, v62, v58, s11
	v_perm_b32 v41, v50, v42, s11
	v_dot4c_i32_i8_e32 v108, v48, v67
	v_perm_b32 v48, v40, v41, s23
	v_perm_b32 v40, v40, v41, s24
	v_dot4c_i32_i8_e32 v103, v60, v67
	v_and_b32_e32 v60, 0xf0f0f0f, v56
	v_dot4c_i32_i8_e32 v97, v56, v67
	v_and_b32_e32 v41, 0xf0f0f0f, v40
	v_perm_b32 v56, v62, v58, s25
	v_perm_b32 v42, v50, v42, s25
	v_perm_b32 v50, v56, v42, s23
	v_perm_b32 v42, v56, v42, s24
	v_dot4c_i32_i8_e32 v117, v41, v67
	v_dot4c_i32_i8_e32 v107, v40, v67
	v_perm_b32 v40, v63, v59, s11
	v_perm_b32 v41, v51, v43, s11
	v_and_b32_e32 v61, 0xf0f0f0f, v49
	v_dot4c_i32_i8_e32 v99, v49, v67
	v_and_b32_e32 v49, 0xf0f0f0f, v48
	v_and_b32_e32 v56, 0xf0f0f0f, v42
	v_dot4c_i32_i8_e32 v111, v42, v67
	v_dot4c_i32_i8_e32 v105, v48, v67
	v_perm_b32 v42, v40, v41, s23
	v_perm_b32 v48, v63, v59, s25
	v_perm_b32 v43, v51, v43, s25
	v_dot4c_i32_i8_e32 v116, v49, v67
	v_perm_b32 v49, v48, v43, s24
	v_perm_b32 v40, v40, v41, s24
	v_and_b32_e32 v41, 0xf0f0f0f, v42
	v_perm_b32 v124, v65, v66, s23
	v_perm_b32 v65, v65, v66, s24
	v_perm_b32 v43, v48, v43, s23
	v_dot4c_i32_i8_e32 v120, v41, v67
	v_and_b32_e32 v41, 0xf0f0f0f, v49
	v_and_b32_e32 v125, 0xf0f0f0f, v124
	v_and_b32_e32 v66, 0xf0f0f0f, v65
	v_dot4c_i32_i8_e32 v112, v57, v67
	v_and_b32_e32 v57, 0xf0f0f0f, v50
	v_dot4c_i32_i8_e32 v113, v40, v67
	v_dot4c_i32_i8_e32 v123, v41, v67
	v_and_b32_e32 v41, 0xf0f0f0f, v43
	v_and_b32_e32 v40, 0xf0f0f0f, v40
	v_dot4c_i32_i8_e32 v102, v66, v67
	v_dot4c_i32_i8_e32 v101, v125, v67
	v_dot4c_i32_i8_e32 v110, v61, v67
	v_dot4c_i32_i8_e32 v106, v60, v67
	v_dot4c_i32_i8_e32 v119, v56, v67
	v_dot4c_i32_i8_e32 v118, v57, v67
	v_dot4c_i32_i8_e32 v122, v41, v67
	v_dot4c_i32_i8_e32 v121, v40, v67
	v_mov_b32_e32 v40, 0
	v_mov_b32_e32 v41, 0
	v_permlane32_swap_b32_e32 v104, v119
	v_mov_b32_dpp v40, v91 row_newbcast:6 row_mask:0xf bank_mask:0x3
	v_mov_b32_dpp v41, v91 row_newbcast:7 row_mask:0xf bank_mask:0x3
	v_permlane32_swap_b32_e32 v103, v118
	v_permlane32_swap_b32_e32 v102, v117
	v_permlane32_swap_b32_e32 v101, v116
	v_permlane32_swap_b32_e32 v112, v123
	v_permlane32_swap_b32_e32 v110, v122
	v_permlane32_swap_b32_e32 v108, v121
	v_permlane32_swap_b32_e32 v106, v120
	v_dot4c_i32_i8_e32 v94, v65, v67
	v_dot4c_i32_i8_e32 v93, v124, v67
	v_dot4c_i32_i8_e32 v109, v50, v67
	v_dot4c_i32_i8_e32 v64, v42, v67
	v_dot4c_i32_i8_e32 v115, v49, v67
	v_dot4c_i32_i8_e32 v114, v43, v67
	v_mov_b32_dpp v40, v91 row_newbcast:14 row_mask:0xf bank_mask:0xc
	v_mov_b32_dpp v41, v91 row_newbcast:15 row_mask:0xf bank_mask:0xc
	v_add_u32_e32 v65, v104, v119
	v_add_u32_e32 v66, v103, v118
	v_add_u32_e32 v67, v102, v117
	v_add_u32_e32 v91, v101, v116
	v_add_u32_e32 v101, v112, v123
	v_add_u32_e32 v102, v110, v122
	v_add_u32_e32 v103, v108, v121
	v_add_u32_e32 v104, v106, v120
	v_permlane16_swap_b32_e32 v65, v101
	v_permlane16_swap_b32_e32 v66, v102
	v_permlane16_swap_b32_e32 v67, v103
	v_permlane16_swap_b32_e32 v91, v104
	v_add_u32_e32 v65, v65, v101
	v_add_u32_e32 v66, v66, v102
	v_add_u32_e32 v67, v67, v103
; __device__ __forceinline__ unsigned pk2(float lo, float hi) { const f32x2_pk v = {lo, hi}; return __builtin_bit_cast(unsigned, __builtin_convertvector(v, bf16x2)); }
; __device__ __forceinline__ float bf_lo(unsigned u) { return __uint_as_float(u << 16); }
; __device__ __forceinline__ float bf_hi(unsigned u) { return __uint_as_float(u & 0xffff0000u); }
; __device__ __forceinline__ void phase_peer_v(Frame& F, bf16_t* XB, const unsigned short* EID, const unsigned char* ACO8, const float* ASC, const unsigned char* V4S, float* SSQP) {
;     ...
;         int L0, L1, P0, P1; red16_groups(oL, b3, L0, L1); red16_groups(oP, b3, P0, P1);
;         const float sc = __uint_as_float(scA.x), corr = __uint_as_float(scA.y);
;         const float f0 = bf_lo(xfA.x) + ((float)L0 * sc - corr), f1 = bf_hi(xfA.x) + (float)((P0 - L0) >> 4) * sc, f2 = bf_lo(xfA.y) + ((float)L1 * sc - corr), f3 = bf_hi(xfA.y) + (float)((P1 - L1) >> 4) * sc;
;         { u32x2 st; st.x = pk2(f0, f1); st.y = pk2(f2, f3); *(u32x2*)(XB + (size_t)t * DM + col) = st; }
;         const float ss = wave_total((f0 * f0 + f1 * f1) + (f2 * f2 + f3 * f3));
;         if (lane == 0) { float* sp = SSQP + (size_t)t * 16 + x; sp[0] = ss; sp[4] = 0.f; sp[8] = 0.f; sp[12] = 0.f; }
	v_add_u32_e32 v91, v91, v104
	v_cndmask_b32_e64 v101, v67, v65, s[2:3]
	v_cndmask_b32_e64 v65, v65, v67, s[2:3]
	v_cndmask_b32_e64 v67, v91, v66, s[2:3]
	v_cndmask_b32_e64 v66, v66, v91, s[2:3]
	v_permlane32_swap_b32_e32 v96, v111
	v_permlane32_swap_b32_e32 v95, v109
	v_permlane32_swap_b32_e32 v94, v107
	v_permlane32_swap_b32_e32 v100, v115
	v_permlane32_swap_b32_e32 v98, v113
	v_add_u32_dpp v67, v66, v67 row_ror:8 row_mask:0xf bank_mask:0xf bound_ctrl:1
	v_add_u32_e32 v66, v96, v111
	v_add_u32_e32 v91, v95, v109
	v_add_u32_e32 v94, v94, v107
	v_permlane32_swap_b32_e32 v93, v105
	v_add_u32_e32 v95, v100, v115
	v_add_u32_e32 v98, v98, v113
	v_permlane32_swap_b32_e32 v97, v64
	v_add_u32_e32 v93, v93, v105
	v_add_u32_e32 v64, v97, v64
	v_permlane16_swap_b32_e32 v66, v95
	v_permlane16_swap_b32_e32 v94, v98
	v_add_u32_dpp v65, v65, v101 row_ror:8 row_mask:0xf bank_mask:0xf bound_ctrl:1
	v_permlane32_swap_b32_e32 v99, v114
	v_add_u32_e32 v66, v66, v95
	v_add_u32_e32 v94, v94, v98
	v_permlane16_swap_b32_e32 v93, v64
	v_add_u32_e32 v96, v99, v114
	v_add_u32_e32 v64, v93, v64
	v_cndmask_b32_e64 v93, v94, v66, s[2:3]
	v_cndmask_b32_e64 v66, v66, v94, s[2:3]
	v_cvt_f32_i32_e32 v94, v65
	v_permlane16_swap_b32_e32 v91, v96
	v_add_u32_e32 v91, v91, v96
	v_sub_u32_dpp v65, v66, v65 row_ror:8 row_mask:0xf bank_mask:0xf bound_ctrl:1
	v_add_u32_e32 v65, v65, v93
	v_cndmask_b32_e64 v93, v64, v91, s[2:3]
	v_cndmask_b32_e64 v91, v91, v64, s[2:3]
	v_fma_f32 v64, v74, v94, -v75
	v_cvt_f32_i32_e32 v94, v67
	v_sub_u32_dpp v67, v91, v67 row_ror:8 row_mask:0xf bank_mask:0xf bound_ctrl:1
	v_ashrrev_i32_e32 v65, 4, v65
	v_add_u32_e32 v67, v67, v93
	v_cvt_f32_i32_e32 v65, v65
	v_ashrrev_i32_e32 v67, 4, v67
	v_cvt_f32_i32_e32 v91, v67
	v_lshlrev_b32_e32 v66, 16, v76
	v_mul_f32_e32 v65, v74, v65
	v_and_b32_e32 v67, 0xffff0000, v76
	v_pk_add_f32 v[64:65], v[64:65], v[66:67]
	v_fma_f32 v66, v74, v94, -v75
	v_mul_f32_e32 v67, v74, v91
	v_lshlrev_b32_e32 v74, 16, v77
	v_and_b32_e32 v75, 0xffff0000, v77
	v_pk_add_f32 v[66:67], v[66:67], v[74:75]
	v_cvt_pk_bf16_f32 v74, v64, v65
	v_cvt_pk_bf16_f32 v75, v66, v67
	v_pk_mul_f32 v[64:65], v[64:65], v[64:65]
	v_pk_mul_f32 v[66:67], v[66:67], v[66:67]
	v_add_f32_e32 v64, v64, v65
	v_add_f32_e32 v66, v66, v67
	v_add_f32_e32 v64, v64, v66
	v_lshlrev_b32_e32 v42, 7, v40
	v_bfe_u32 v40, v40, 16, 16
	v_add_f32_dpp v64, v64, v64 row_shr:1 row_mask:0xf bank_mask:0xf bound_ctrl:1
	v_lshl_or_b32 v48, v40, 7, v90
	v_lshlrev_b32_e32 v40, 7, v41
	v_add_f32_dpp v64, v64, v64 row_shr:2 row_mask:0xf bank_mask:0xf bound_ctrl:1
	v_and_or_b32 v42, v42, s22, v90
	v_and_or_b32 v56, v40, s22, v90
	v_bfe_u32 v40, v41, 16, 16
	v_add_f32_dpp v64, v64, v64 row_shr:4 row_mask:0xf bank_mask:0xf bound_ctrl:1
	v_lshl_or_b32 v60, v40, 7, v90
	global_load_dwordx4 v[40:43], v42, s[8:9]
	v_mov_b32_e32 v65, 0
	v_add_f32_dpp v64, v64, v64 row_shr:8 row_mask:0xf bank_mask:0xf bound_ctrl:1
	global_load_dwordx4 v[48:51], v48, s[8:9]
	global_load_dwordx4 v[56:59], v56, s[8:9]
	global_load_dwordx4 v[60:63], v60, s[8:9]
	v_lshl_add_u64 v[76:77], s[78:79], 0, v[84:85]
	global_store_dwordx2 v[76:77], v[74:75], off
	v_mov_b32_dpp v65, v64 row_bcast:15 row_mask:0xa bank_mask:0xf
	v_add_f32_e32 v64, v64, v65
	v_mov_b32_e32 v65, 0
	s_nop 1
	v_mov_b32_dpp v65, v64 row_bcast:31 row_mask:0xc bank_mask:0xf
	v_add_f32_e32 v64, v64, v65
	s_nop 0
	v_readlane_b32 s26, v64, 63
	s_and_saveexec_b64 s[20:21], s[4:5]
	s_cbranch_execz .LBB0_1007
	s_add_u32 s28, s78, s12
	s_addc_u32 s29, s79, s13
	s_mov_b64 exec, 15
	s_nop 4
	v_mov_b32_dpp v65, v72 quad_perm:[0,0,0,0] row_mask:0x1 bank_mask:0x1
	v_mov_b32_e32 v64, 0
	s_nop 0
	v_writelane_b32 v64, s26, 0
	v_lshl_add_u32 v65, v208, 4, v65
	global_store_dword v65, v64, s[28:29]
	s_branch .LBB0_1007
